# combine phase: also touch the next iteration's top-k index lines (6 dummy dword loads) after the current index wait
# baseline (speedup 1.0000x reference)
.LBB0_1397:
	s_add_i32 s39, s33, s2
	s_cmpk_lt_i32 s39, 0x4000
	s_cselect_b32 s16, s39, s2
	s_lshl_b32 s18, s16, 2
	s_ashr_i32 s17, s16, 31
	s_ashr_i32 s19, s18, 31
	s_lshl_b64 s[0:1], s[16:17], 11
	s_lshl_b64 s[16:17], s[18:19], 2
	s_add_u32 s22, s40, s16
	s_addc_u32 s23, s41, s17
	s_add_u32 s20, s44, s16
	s_addc_u32 s21, s45, s17
	s_add_u32 s16, s36, s16
	s_addc_u32 s17, s37, s17
	s_or_b32 s18, s18, 2
	s_ashr_i32 s19, s18, 31
	s_lshl_b64 s[18:19], s[18:19], 2
	s_add_u32 s18, s36, s18
	s_addc_u32 s19, s37, s19
	s_ashr_i32 s15, s14, 31
	global_load_dwordx4 v[0:3], v9, s[22:23]
	s_add_i32 s30, s14, -3
	s_lshl_b64 s[22:23], s[14:15], 2
	s_add_u32 s34, s44, s22
	s_addc_u32 s35, s45, s23
	s_add_u32 s26, s40, s22
	s_addc_u32 s27, s41, s23
	s_add_i32 s24, s14, -1
	s_ashr_i32 s25, s24, 31
	s_lshl_b64 s[24:25], s[24:25], 2
	s_add_u32 s42, s44, s24
	s_addc_u32 s43, s45, s25
	s_add_u32 s28, s40, s24
	s_addc_u32 s29, s41, s25
	global_load_dword v19, v9, s[26:27]
	global_load_dword v25, v9, s[28:29]
	s_add_i32 s26, s14, -2
	s_ashr_i32 s27, s26, 31
	s_lshl_b64 s[26:27], s[26:27], 2
	s_add_u32 s28, s44, s26
	s_addc_u32 s29, s45, s27
	s_add_u32 s46, s40, s26
	s_addc_u32 s47, s41, s27
	global_load_dword v38, v9, s[46:47]
	global_load_dword v39, v9, s[42:43]
	global_load_dword v40, v9, s[34:35]
	s_ashr_i32 s31, s30, 31
	s_lshl_b64 s[30:31], s[30:31], 2
	s_add_u32 s34, s44, s30
	s_addc_u32 s35, s45, s31
	s_add_u32 s42, s40, s30
	s_addc_u32 s43, s41, s31
	global_load_dword v41, v9, s[42:43]
	global_load_dword v42, v9, s[28:29]
	global_load_dword v43, v9, s[34:35]
	global_load_dwordx2 v[26:27], v[16:17], off offset:1536 nt
	global_load_dwordx2 v[36:37], v[16:17], off offset:1024 nt
	global_load_dwordx2 v[20:21], v[16:17], off offset:512 nt
	global_load_dwordx4 v[4:7], v9, s[20:21]
	s_add_u32 s20, s36, s22
	s_addc_u32 s21, s37, s23
	s_add_u32 s22, s36, s24
	s_addc_u32 s23, s37, s25
	global_load_dword v18, v9, s[20:21]
	s_add_u32 s20, s36, s26
	s_addc_u32 s21, s37, s27
	s_add_u32 s24, s36, s30
	s_addc_u32 s25, s37, s31
	global_load_dword v24, v9, s[22:23]
	global_load_dword v22, v9, s[20:21]
	global_load_dword v23, v9, s[24:25]
	s_cmpk_gt_i32 s39, 0x3fff
	s_waitcnt vmcnt(0)
	s_cselect_b32 s99, 1, 0
	s_add_i32 s98, s2, s4
	s_lshl_b32 s98, s98, 4
	s_add_u32 s100, s40, s98
	s_addc_u32 s101, s41, 0
	global_load_dword v199, v9, s[100:101]
	s_add_u32 s100, s44, s98
	s_addc_u32 s101, s45, 0
	global_load_dword v199, v9, s[100:101]
	s_add_u32 s100, s36, s98
	s_addc_u32 s101, s37, 0
	global_load_dword v199, v9, s[100:101]
	s_lshl_b32 s100, s33, 4
	s_add_u32 s98, s98, s100
	s_add_u32 s100, s40, s98
	s_addc_u32 s101, s41, 0
	global_load_dword v199, v9, s[100:101]
	s_add_u32 s100, s44, s98
	s_addc_u32 s101, s45, 0
	global_load_dword v199, v9, s[100:101]
	s_add_u32 s100, s36, s98
	s_addc_u32 s101, s37, 0
	global_load_dword v199, v9, s[100:101]
	s_cmp_lg_u32 s99, 0
	v_lshlrev_b32_e32 v1, 2, v1
	v_lshlrev_b32_e32 v2, 2, v2
	v_lshlrev_b32_e32 v3, 2, v3
	v_add_u32_e32 v1, s5, v1
	v_add_u32_e32 v2, s5, v2
	v_add_u32_e32 v3, s5, v3
	v_lshlrev_b32_e32 v0, 2, v0
	v_add_u32_e32 v0, s5, v0
	v_lshlrev_b32_e32 v19, 2, v19
	v_lshlrev_b32_e32 v25, 2, v25
	v_add_u32_e32 v19, s5, v19
	v_add_u32_e32 v25, s5, v25
	v_lshlrev_b32_e32 v38, 2, v38
	v_add_u32_e32 v38, s5, v38
	ds_read_b32 v1, v1
	ds_read_b32 v25, v25
	ds_read_b32 v114, v2
	ds_read_b32 v115, v3
	ds_read_b32 v19, v19
	ds_read_b32 v44, v38
	s_waitcnt lgkmcnt(0)
	v_add_u32_e32 v2, v39, v25
	v_ashrrev_i32_e32 v3, 31, v2
	v_lshlrev_b64 v[2:3], 10, v[2:3]
	v_lshl_add_u64 v[38:39], v[14:15], 0, v[2:3]
	global_load_dword v60, v[38:39], off offset:768 nt
	global_load_dword v48, v[38:39], off nt
	global_load_dword v56, v[38:39], off offset:512 nt
	global_load_dword v52, v[38:39], off offset:256 nt
	global_load_dwordx2 v[2:3], v9, s[18:19]
	v_add_u32_e32 v38, v40, v19
	v_ashrrev_i32_e32 v39, 31, v38
	v_lshlrev_b64 v[38:39], 10, v[38:39]
	v_lshlrev_b32_e32 v19, 2, v41
	v_lshl_add_u64 v[38:39], v[14:15], 0, v[38:39]
	v_add_u32_e32 v19, s5, v19
	global_load_dword v64, v[38:39], off nt
	global_load_dword v68, v[38:39], off offset:256 nt
	global_load_dword v72, v[38:39], off offset:512 nt
	ds_read_b32 v19, v19
	v_add_u32_e32 v40, v42, v44
	v_ashrrev_i32_e32 v41, 31, v40
	v_lshlrev_b64 v[40:41], 10, v[40:41]
	v_lshl_add_u64 v[40:41], v[14:15], 0, v[40:41]
	s_waitcnt lgkmcnt(0)
	v_add_u32_e32 v42, v43, v19
	v_ashrrev_i32_e32 v43, 31, v42
	v_lshlrev_b64 v[42:43], 10, v[42:43]
	global_load_dword v74, v[40:41], off offset:768 nt
	v_lshl_add_u64 v[42:43], v[14:15], 0, v[42:43]
	global_load_dword v86, v[42:43], off nt
	global_load_dword v90, v[42:43], off offset:256 nt
	global_load_dword v94, v[42:43], off offset:512 nt
	global_load_dword v98, v[42:43], off offset:768 nt
	global_load_dword v102, v[40:41], off nt
	global_load_dword v106, v[40:41], off offset:256 nt
	global_load_dword v110, v[40:41], off offset:512 nt
	global_load_dword v116, v[38:39], off offset:768 nt
	global_load_dwordx2 v[44:45], v[16:17], off nt
	v_lshlrev_b32_e32 v40, 16, v36
	v_lshlrev_b32_e32 v119, 16, v20
	v_and_b32_e32 v20, 0xffff0000, v20
	v_lshlrev_b32_e32 v38, 16, v26
	v_lshlrev_b32_e32 v42, 16, v37
	v_mov_b32_e32 v25, v22
	v_and_b32_e32 v117, 0xffff0000, v36
	v_mov_b32_e32 v19, v24
	v_and_b32_e32 v39, 0xffff0000, v26
	v_lshlrev_b32_e32 v41, 16, v27
	v_and_b32_e32 v43, 0xffff0000, v27
	v_mov_b32_e32 v27, v22
	v_mov_b32_e32 v26, v23
	v_and_b32_e32 v118, 0xffff0000, v37
	v_mov_b32_e32 v37, v18
	v_mov_b32_e32 v36, v24
	s_waitcnt vmcnt(17)
	v_cvt_pk_f32_fp8_e32 v[58:59], v60
	s_waitcnt vmcnt(16)
	v_cvt_pk_f32_fp8_e32 v[46:47], v48
	s_waitcnt vmcnt(15)
	v_cvt_pk_f32_fp8_e32 v[54:55], v56
	s_waitcnt vmcnt(14)
	v_cvt_pk_f32_fp8_e32 v[50:51], v52
	v_cvt_pk_f32_fp8_sdwa v[52:53], v52 src0_sel:WORD_1
	v_mul_f32_e32 v75, v24, v59
	v_cvt_pk_f32_fp8_sdwa v[56:57], v56 src0_sel:WORD_1
	v_mov_b32_e32 v77, v51
	v_mov_b32_e32 v78, v52
	s_waitcnt vmcnt(12)
	v_cvt_pk_f32_fp8_e32 v[62:63], v64
	s_waitcnt vmcnt(11)
	v_cvt_pk_f32_fp8_e32 v[66:67], v68
	v_cvt_pk_f32_fp8_sdwa v[68:69], v68 src0_sel:WORD_1
	s_waitcnt vmcnt(10)
	v_cvt_pk_f32_fp8_e32 v[70:71], v72
	v_cvt_pk_f32_fp8_sdwa v[72:73], v72 src0_sel:WORD_1
	s_waitcnt vmcnt(8)
	v_cvt_pk_f32_fp8_e32 v[84:85], v86
	s_waitcnt vmcnt(7)
	v_cvt_pk_f32_fp8_e32 v[88:89], v90
	s_waitcnt vmcnt(6)
	v_cvt_pk_f32_fp8_e32 v[92:93], v94
	v_cvt_pk_f32_fp8_sdwa v[90:91], v90 src0_sel:WORD_1
	v_cvt_pk_f32_fp8_sdwa v[94:95], v94 src0_sel:WORD_1
	s_waitcnt vmcnt(3)
	v_cvt_pk_f32_fp8_e32 v[104:105], v106
	v_cvt_pk_f32_fp8_e32 v[80:81], v74
	s_waitcnt vmcnt(2)
	v_cvt_pk_f32_fp8_e32 v[108:109], v110
	v_cvt_pk_f32_fp8_e32 v[96:97], v98
	v_mov_b32_e32 v113, v88
	v_mov_b32_e32 v88, v105
	v_cvt_pk_f32_fp8_e32 v[100:101], v102
	v_cvt_pk_f32_fp8_sdwa v[106:107], v106 src0_sel:WORD_1
	v_cvt_pk_f32_fp8_sdwa v[110:111], v110 src0_sel:WORD_1
	v_pk_mul_f32 v[88:89], v[22:23], v[88:89]
	v_mov_b32_e32 v59, v80
	v_fmac_f32_e32 v40, v23, v92
	v_mov_b32_e32 v112, v104
	v_mov_b32_e32 v92, v109
	v_add_f32_e32 v20, v89, v20
	v_pk_mul_f32 v[58:59], v[24:25], v[58:59]
	v_fmac_f32_e32 v42, v23, v94
	v_fmac_f32_e32 v38, v23, v96
	v_mov_b32_e32 v104, v90
	v_mov_b32_e32 v90, v95
	v_pk_mul_f32 v[94:95], v[22:23], v[112:113]
	v_pk_mul_f32 v[92:93], v[22:23], v[92:93]
	v_add_f32_e32 v20, v88, v20
	s_waitcnt vmcnt(0)
	v_lshlrev_b32_e32 v88, 16, v44
	v_and_b32_e32 v89, 0xffff0000, v44
	v_mov_b32_e32 v44, v23
	v_mov_b32_e32 v79, v68
	v_mov_b32_e32 v68, v53
	v_mov_b32_e32 v52, v71
	v_mov_b32_e32 v53, v55
	v_cvt_pk_f32_fp8_sdwa v[86:87], v86 src0_sel:WORD_1
	v_cvt_pk_f32_fp8_sdwa v[98:99], v98 src0_sel:WORD_1
	v_add_f32_e32 v38, v59, v38
	v_add_f32_e32 v51, v95, v119
	v_add_f32_e32 v55, v93, v117
	v_pk_fma_f32 v[84:85], v[44:45], v[84:85], v[88:89] op_sel_hi:[0,1,1]
	v_cvt_pk_f32_fp8_sdwa v[82:83], v74 src0_sel:WORD_1
	v_pk_mul_f32 v[52:53], v[18:19], v[52:53]
	v_cvt_pk_f32_fp8_sdwa v[102:103], v102 src0_sel:WORD_1
	v_mov_b32_e32 v105, v106
	v_mov_b32_e32 v106, v91
	v_mov_b32_e32 v91, v111
	v_add_f32_e32 v59, v58, v38
	v_add_f32_e32 v38, v94, v51
	v_add_f32_e32 v51, v92, v55
	v_pk_fma_f32 v[84:85], v[22:23], v[100:101], v[84:85] op_sel_hi:[0,1,1]
	v_cvt_pk_f32_fp8_sdwa v[48:49], v48 src0_sel:WORD_1
	v_mov_b32_e32 v76, v67
	v_pk_mul_f32 v[104:105], v[26:27], v[104:105]
	v_pk_mul_f32 v[106:107], v[26:27], v[106:107]
	v_pk_mul_f32 v[26:27], v[26:27], v[90:91]
	v_add_f32_e32 v51, v53, v51
	v_pk_fma_f32 v[46:47], v[24:25], v[46:47], v[84:85] op_sel_hi:[0,1,1]
	v_cvt_pk_f32_fp8_sdwa v[60:61], v60 src0_sel:WORD_1
	v_pk_mul_f32 v[76:77], v[18:19], v[76:77]
	v_add_f32_e32 v26, v26, v118
	v_add_f32_e32 v80, v52, v51
	v_mov_b32_e32 v52, v57
	v_mov_b32_e32 v53, v73
	v_pk_fma_f32 v[62:63], v[18:19], v[62:63], v[46:47] op_sel_hi:[0,1,1]
	v_lshlrev_b32_e32 v46, 16, v45
	v_and_b32_e32 v47, 0xffff0000, v45
	v_pk_mul_f32 v[78:79], v[36:37], v[78:79]
	v_pk_mul_f32 v[68:69], v[36:37], v[68:69]
	v_add_f32_e32 v27, v26, v27
	v_add_f32_e32 v20, v77, v20
	v_pk_mul_f32 v[36:37], v[36:37], v[52:53]
	v_pk_fma_f32 v[44:45], v[44:45], v[86:87], v[46:47] op_sel_hi:[0,1,1]
	v_mov_b32_e32 v109, v98
	v_mov_b32_e32 v111, v99
	v_add_f32_e32 v26, v76, v20
	v_cvt_pk_f32_fp8_sdwa v[52:53], v116 src0_sel:WORD_1
	v_add_f32_e32 v20, v27, v36
	v_pk_fma_f32 v[44:45], v[22:23], v[102:103], v[44:45] op_sel_hi:[0,1,1]
	v_pk_fma_f32 v[40:41], v[22:23], v[108:109], v[40:41]
	v_pk_fma_f32 v[42:43], v[22:23], v[110:111], v[42:43]
	v_mov_b32_e32 v46, v24
	v_mov_b32_e32 v47, v23
	v_mov_b32_e32 v51, v97
	v_mov_b32_e32 v55, v82
	v_mov_b32_e32 v57, v83
	v_add_f32_e32 v90, v20, v37
	v_cvt_pk_f32_fp8_e32 v[36:37], v116
	v_pk_fma_f32 v[44:45], v[24:25], v[48:49], v[44:45] op_sel_hi:[0,1,1]
	v_pk_fma_f32 v[38:39], v[46:47], v[50:51], v[38:39]
	v_pk_fma_f32 v[40:41], v[24:25], v[54:55], v[40:41]
	v_pk_fma_f32 v[24:25], v[24:25], v[56:57], v[42:43]
	v_mov_b32_e32 v42, v18
	v_mov_b32_e32 v43, v22
	v_mov_b32_e32 v67, v81
	v_pk_fma_f32 v[54:55], v[42:43], v[66:67], v[38:39]
	v_mov_b32_e32 v71, v60
	v_pk_fma_f32 v[56:57], v[18:19], v[70:71], v[40:41]
	v_mov_b32_e32 v73, v61
	v_mov_b32_e32 v74, v54
	v_cvt_pk_f32_fp8_sdwa v[64:65], v64 src0_sel:WORD_1
	v_mul_f32_e32 v77, v18, v52
	v_pk_fma_f32 v[60:61], v[18:19], v[72:73], v[24:25]
	v_pk_mul_f32 v[22:23], v[54:55], v[54:55]
	v_pk_add_f32 v[24:25], v[54:55], v[74:75]
	v_mov_b32_e32 v76, v56
	v_mul_f32_e32 v53, v18, v53
	v_mul_f32_e32 v20, v80, v80
	v_mov_b32_e32 v23, v25
	v_mov_b32_e32 v27, v18
	v_mov_b32_e32 v38, v26
	v_mov_b32_e32 v39, v37
	v_pk_add_f32 v[48:49], v[56:57], v[76:77]
	v_mov_b32_e32 v52, v60
	v_mul_f32_e32 v58, v90, v90
	v_pk_fma_f32 v[66:67], v[26:27], v[38:39], v[22:23]
	v_pk_add_f32 v[70:71], v[60:61], v[52:53]
	v_pk_fma_f32 v[22:23], v[56:57], v[56:57], v[20:21]
	v_pk_mul_f32 v[38:39], v[48:49], v[48:49]
	v_pk_mul_f32 v[40:41], v[70:71], v[70:71]
	v_mov_b32_e32 v23, v39
	v_pk_fma_f32 v[38:39], v[60:61], v[60:61], v[58:59]
	v_pk_fma_f32 v[64:65], v[18:19], v[64:65], v[44:45] op_sel_hi:[0,1,1]
	v_mov_b32_e32 v39, v41
	v_pk_mul_f32 v[44:45], v[64:65], v[64:65]
	v_pk_add_f32 v[22:23], v[22:23], v[38:39]
	v_mov_b32_e32 v38, v62
	v_mov_b32_e32 v39, v18
	v_mov_b32_e32 v40, v62
	v_mov_b32_e32 v41, v36
	v_mul_f32_e32 v58, v63, v63
	v_mov_b32_e32 v42, v64
	v_mov_b32_e32 v43, v18
	v_mov_b32_e32 v46, v64
	v_mov_b32_e32 v47, v36
	v_pk_fma_f32 v[72:73], v[38:39], v[40:41], v[58:59]
	v_mov_b32_e32 v58, v45
	v_pk_fma_f32 v[38:39], v[42:43], v[46:47], v[58:59]
	v_lshlrev_b32_e32 v20, 16, v21
	v_pk_add_f32 v[40:41], v[72:73], v[38:39]
	v_pk_mul_f32 v[38:39], v[72:73], v[38:39]
	v_and_b32_e32 v21, 0xffff0000, v21
	v_mov_b32_e32 v41, v39
	v_mov_b32_e32 v38, v104
	v_mov_b32_e32 v39, v106
	v_pk_add_f32 v[20:21], v[38:39], v[20:21]
	v_mov_b32_e32 v106, v105
	v_pk_add_f32 v[20:21], v[20:21], v[106:107]
	v_mov_b32_e32 v38, v78
	v_mov_b32_e32 v39, v68
	v_pk_add_f32 v[20:21], v[20:21], v[38:39]
	v_mov_b32_e32 v68, v79
	v_pk_add_f32 v[58:59], v[20:21], v[68:69]
	v_lshl_add_u64 v[38:39], v[12:13], 0, s[0:1]
	v_pk_mul_f32 v[20:21], v[58:59], v[58:59]
	v_pk_mov_b32 v[18:19], v[58:59], v[18:19] op_sel:[1,0]
	v_mov_b32_e32 v36, v59
	v_mov_b32_e32 v21, v25
	v_pk_fma_f32 v[18:19], v[18:19], v[36:37], v[20:21]
	s_nop 0
	v_pk_add_f32 v[20:21], v[66:67], v[18:19]
	v_pk_mul_f32 v[18:19], v[66:67], v[18:19]
	s_nop 0
	v_mov_b32_e32 v21, v19
	v_pk_add_f32 v[18:19], v[40:41], v[20:21]
	s_nop 0
	v_pk_add_f32 v[18:19], v[18:19], v[22:23]
	ds_read_b32 v22, v0
	v_add_f32_e32 v18, v18, v19
	ds_bpermute_b32 v19, v28, v18
	v_add_u32_e32 v0, v5, v1
	v_ashrrev_i32_e32 v1, 31, v0
	s_waitcnt lgkmcnt(1)
	v_add_u32_e32 v4, v4, v22
	v_ashrrev_i32_e32 v5, 31, v4
	s_waitcnt lgkmcnt(0)
	v_add_f32_e32 v23, v18, v19
	global_load_dwordx2 v[20:21], v9, s[16:17]
	global_load_dwordx2 v[18:19], v9, s[16:17] offset:4
	ds_bpermute_b32 v24, v29, v23
	v_lshlrev_b64 v[36:37], 10, v[4:5]
	v_add_u32_e32 v4, v6, v114
	v_ashrrev_i32_e32 v5, 31, v4
	v_lshlrev_b64 v[68:69], 10, v[4:5]
	s_waitcnt lgkmcnt(0)
	v_add_f32_e32 v23, v23, v24
	ds_bpermute_b32 v27, v30, v23
	v_lshlrev_b64 v[24:25], 10, v[0:1]
	v_add_u32_e32 v0, v7, v115
	v_lshl_add_u64 v[36:37], v[14:15], 0, v[36:37]
	v_lshl_add_u64 v[24:25], v[14:15], 0, v[24:25]
	s_waitcnt lgkmcnt(0)
	v_add_f32_e32 v1, v23, v27
	ds_bpermute_b32 v22, v31, v1
	v_lshl_add_u64 v[68:69], v[14:15], 0, v[68:69]
	s_waitcnt lgkmcnt(0)
	v_add_f32_e32 v6, v1, v22
	ds_bpermute_b32 v7, v32, v6
	v_ashrrev_i32_e32 v1, 31, v0
	v_lshlrev_b64 v[40:41], 10, v[0:1]
	v_lshl_add_u64 v[74:75], v[14:15], 0, v[40:41]
	s_waitcnt lgkmcnt(0)
	v_add_f32_e32 v27, v6, v7
	ds_bpermute_b32 v42, v33, v27
	global_load_dwordx2 v[4:5], v[38:39], off nt
	global_load_dwordx2 v[0:1], v[38:39], off offset:512 nt
	global_load_dwordx2 v[6:7], v[38:39], off offset:1024 nt
	global_load_dwordx2 v[22:23], v[38:39], off offset:1536 nt
	s_waitcnt lgkmcnt(0)
	v_add_f32_e32 v27, v27, v42
	v_fmamk_f32 v27, v27, 0x3a800000, v34
	v_mul_f32_e32 v38, 0x4f800000, v27
	v_cmp_gt_f32_e32 vcc, s38, v27
	s_nop 1
	v_cndmask_b32_e32 v39, v27, v38, vcc
	v_sqrt_f32_e32 v42, v39
	global_load_dword v48, v[36:37], off nt
	global_load_dword v46, v[36:37], off offset:256 nt
	global_load_dword v47, v[36:37], off offset:512 nt
	global_load_dword v45, v[36:37], off offset:768 nt
	global_load_dword v44, v[24:25], off nt
	global_load_dword v43, v[24:25], off offset:256 nt
	global_load_dword v38, v[24:25], off offset:512 nt
	global_load_dword v27, v[24:25], off offset:768 nt
	v_add_u32_e32 v24, -1, v42
	v_fma_f32 v25, -v24, v42, v39
	v_cmp_ge_f32_e64 s[0:1], 0, v25
	v_add_u32_e32 v25, 1, v42
	v_fma_f32 v36, -v25, v42, v39
	v_cndmask_b32_e64 v24, v42, v24, s[0:1]
	v_cmp_lt_f32_e64 s[0:1], 0, v36
	s_nop 1
	v_cndmask_b32_e64 v24, v24, v25, s[0:1]
	v_mul_f32_e32 v25, 0x37800000, v24
	v_cndmask_b32_e32 v24, v24, v25, vcc
	v_cmp_class_f32_e32 vcc, v39, v35
	s_nop 1
	v_cndmask_b32_e32 v55, v24, v39, vcc
	v_div_scale_f32 v57, s[0:1], v55, v55, 1.0
	v_rcp_f32_e32 v61, v57
	global_load_dword v42, v[68:69], off nt
	global_load_dword v41, v[68:69], off offset:256 nt
	global_load_dword v40, v[68:69], off offset:512 nt
	global_load_dword v39, v[68:69], off offset:768 nt
	global_load_dword v36, v[74:75], off nt
	global_load_dword v37, v[74:75], off offset:256 nt
	global_load_dword v25, v[74:75], off offset:512 nt
	global_load_dword v24, v[74:75], off offset:768 nt
	v_lshl_add_u64 v[68:69], s[10:11], 0, v[8:9]
	v_fma_f32 v66, -v57, v61, 1.0
	v_fmac_f32_e32 v61, v66, v61
	v_div_scale_f32 v66, vcc, 1.0, v55, 1.0
	v_mul_f32_e32 v70, v66, v61
	v_fma_f32 v72, -v57, v70, v66
	v_fmac_f32_e32 v70, v72, v61
	v_fma_f32 v57, -v57, v70, v66
	v_div_fmas_f32 v57, v57, v61, v70
	v_div_fixup_f32 v72, v57, v55, 1.0
	v_pk_mul_f32 v[62:63], v[72:73], v[62:63] op_sel_hi:[0,1]
	v_pk_mul_f32 v[64:65], v[72:73], v[64:65] op_sel_hi:[0,1]
	v_mov_b32_e32 v55, v26
	v_pk_mul_f32 v[58:59], v[72:73], v[58:59] op_sel_hi:[0,1]
	v_pk_mul_f32 v[54:55], v[72:73], v[54:55] op_sel_hi:[0,1]
	v_mov_b32_e32 v57, v80
	v_mov_b32_e32 v61, v90
	s_waitcnt vmcnt(20)
	v_pk_mul_f32 v[52:53], v[202:203], v[64:65]
	v_pk_mul_f32 v[50:51], v[200:201], v[62:63]
	global_store_dwordx4 v[68:69], v[50:53], off nt
	v_pk_mul_f32 v[56:57], v[72:73], v[56:57] op_sel_hi:[0,1]
	v_mov_b32_e32 v70, v49
	v_mov_b32_e32 v66, v73
	v_pk_mul_f32 v[50:51], v[204:205], v[54:55]
	v_pk_mul_f32 v[52:53], v[206:207], v[58:59]
	global_store_dwordx4 v[68:69], v[50:53], off offset:1024 nt
	v_pk_mul_f32 v[54:55], v[72:73], v[60:61] op_sel_hi:[0,1]
	s_nop 1
	v_pk_mul_f32 v[50:51], v[208:209], v[56:57]
	v_pk_mul_f32 v[52:53], v[210:211], v[54:55]
	global_store_dwordx4 v[68:69], v[50:53], off offset:2048 nt
	v_pk_mul_f32 v[54:55], v[72:73], v[66:67] op_sel_hi:[0,1]
	v_pk_mul_f32 v[56:57], v[72:73], v[70:71] op_sel_hi:[0,1]
	v_pk_mul_f32 v[50:51], v[212:213], v[54:55]
	v_pk_mul_f32 v[52:53], v[214:215], v[56:57]
	global_store_dwordx4 v[68:69], v[50:53], off offset:3072 nt
	s_waitcnt vmcnt(4)
	s_cbranch_scc1 .LBB0_1396
	s_nop 0
	v_and_b32_e32 v51, 0xffff0000, v23
	v_lshlrev_b32_e32 v53, 16, v23
	v_and_b32_e32 v49, 0xffff0000, v22
	v_lshlrev_b32_e32 v82, 16, v22
	v_cvt_pk_f32_fp8_e32 v[22:23], v46
	v_cvt_pk_f32_fp8_e32 v[66:67], v43
	v_mov_b32_e32 v70, v18
	v_mov_b32_e32 v71, v20
	v_mov_b32_e32 v73, v22
	v_mov_b32_e32 v72, v66
	v_and_b32_e32 v75, 0xffff0000, v0
	v_lshlrev_b32_e32 v0, 16, v0
	v_cvt_pk_f32_fp8_e32 v[56:57], v47
	v_cvt_pk_f32_fp8_sdwa v[58:59], v47 src0_sel:WORD_1
	v_cvt_pk_f32_fp8_sdwa v[46:47], v46 src0_sel:WORD_1
	v_cvt_pk_f32_fp8_sdwa v[68:69], v43 src0_sel:WORD_1
	v_pk_mul_f32 v[72:73], v[70:71], v[72:73]
	v_mov_b32_e32 v22, v67
	v_add_f32_e32 v0, v73, v0
	v_and_b32_e32 v26, 0xffff0000, v7
	v_lshlrev_b32_e32 v50, 16, v7
	v_and_b32_e32 v74, 0xffff0000, v6
	v_lshlrev_b32_e32 v52, 16, v6
	v_cvt_pk_f32_fp8_e32 v[6:7], v48
	v_cvt_pk_f32_fp8_sdwa v[54:55], v48 src0_sel:WORD_1
	v_add_f32_e32 v48, v72, v0
	v_pk_mul_f32 v[22:23], v[70:71], v[22:23]
	v_cvt_pk_f32_fp8_e32 v[72:73], v38
	v_add_f32_e32 v0, v23, v75
	v_add_f32_e32 v0, v22, v0
	v_mov_b32_e32 v22, v20
	v_mov_b32_e32 v23, v18
	v_mov_b32_e32 v67, v68
	v_mov_b32_e32 v68, v47
	v_cvt_pk_f32_fp8_e32 v[60:61], v45
	v_mov_b32_e32 v66, v46
	v_pk_mul_f32 v[46:47], v[22:23], v[68:69]
	v_cvt_pk_f32_fp8_sdwa v[68:69], v38 src0_sel:WORD_1
	v_fmac_f32_e32 v52, v20, v56
	v_mov_b32_e32 v56, v73
	v_pk_mul_f32 v[56:57], v[70:71], v[56:57]
	v_fmac_f32_e32 v82, v20, v60
	v_add_f32_e32 v38, v57, v74
	v_add_f32_e32 v60, v56, v38
	v_mov_b32_e32 v56, v59
	v_mov_b32_e32 v57, v69
	v_pk_mul_f32 v[66:67], v[22:23], v[66:67]
	v_pk_mul_f32 v[22:23], v[22:23], v[56:57]
	v_cvt_pk_f32_fp8_e32 v[56:57], v27
	v_cvt_pk_f32_fp8_e32 v[76:77], v39
	v_mov_b32_e32 v78, v2
	v_mov_b32_e32 v79, v18
	v_mov_b32_e32 v81, v56
	v_mov_b32_e32 v80, v76
	v_cvt_pk_f32_fp8_e32 v[70:71], v41
	v_pk_mul_f32 v[78:79], v[78:79], v[80:81]
	v_cvt_pk_f32_fp8_e32 v[80:81], v37
	v_add_f32_e32 v22, v22, v26
	v_add_f32_e32 v69, v22, v23
	v_cvt_pk_f32_fp8_sdwa v[22:23], v41 src0_sel:WORD_1
	v_add_f32_e32 v56, v79, v82
	v_cvt_pk_f32_fp8_e32 v[82:83], v36
	v_cvt_pk_f32_fp8_sdwa v[84:85], v36 src0_sel:WORD_1
	v_cvt_pk_f32_fp8_sdwa v[36:37], v37 src0_sel:WORD_1
	v_cvt_pk_f32_fp8_e32 v[74:75], v40
	v_cvt_pk_f32_fp8_e32 v[88:89], v25
	v_mov_b32_e32 v86, v81
	v_mov_b32_e32 v87, v71
	v_pk_mul_f32 v[86:87], v[2:3], v[86:87] op_sel:[1,0] op_sel_hi:[0,1]
	v_cvt_pk_f32_fp8_sdwa v[40:41], v40 src0_sel:WORD_1
	v_add_f32_e32 v0, v87, v0
	v_mov_b32_e32 v87, v22
	v_mov_b32_e32 v22, v37
	v_cvt_pk_f32_fp8_sdwa v[90:91], v25 src0_sel:WORD_1
	v_add_f32_e32 v79, v78, v56
	v_add_f32_e32 v56, v86, v0
	v_mov_b32_e32 v86, v36
	v_pk_mul_f32 v[36:37], v[2:3], v[22:23] op_sel:[1,0] op_sel_hi:[0,1]
	v_mov_b32_e32 v22, v89
	v_mov_b32_e32 v23, v75
	v_cvt_pk_f32_fp8_sdwa v[62:63], v45 src0_sel:WORD_1
	v_pk_mul_f32 v[22:23], v[2:3], v[22:23] op_sel:[1,0] op_sel_hi:[0,1]
	v_cvt_pk_f32_fp8_e32 v[64:65], v44
	v_cvt_pk_f32_fp8_sdwa v[44:45], v44 src0_sel:WORD_1
	v_cvt_pk_f32_fp8_sdwa v[26:27], v27 src0_sel:WORD_1
	v_add_f32_e32 v0, v23, v60
	v_add_f32_e32 v100, v22, v0
	v_mov_b32_e32 v22, v91
	v_mov_b32_e32 v23, v41
	v_pk_mul_f32 v[22:23], v[2:3], v[22:23] op_sel:[1,0] op_sel_hi:[0,1]
	v_lshlrev_b32_e32 v98, 16, v4
	v_and_b32_e32 v99, 0xffff0000, v4
	v_lshlrev_b32_e32 v4, 16, v5
	v_and_b32_e32 v5, 0xffff0000, v5
	v_fmac_f32_e32 v50, v20, v58
	v_add_f32_e32 v0, v69, v23
	v_pk_fma_f32 v[4:5], v[20:21], v[54:55], v[4:5] op_sel_hi:[0,1,1]
	v_mov_b32_e32 v73, v62
	v_mov_b32_e32 v69, v63
	v_cvt_pk_f32_fp8_sdwa v[38:39], v39 src0_sel:WORD_1
	v_pk_fma_f32 v[4:5], v[18:19], v[44:45], v[4:5] op_sel_hi:[0,1,1]
	v_pk_fma_f32 v[44:45], v[20:21], v[72:73], v[52:53] op_sel:[1,0,0] op_sel_hi:[0,1,1]
	v_pk_fma_f32 v[50:51], v[20:21], v[68:69], v[50:51] op_sel:[1,0,0] op_sel_hi:[0,1,1]
	v_mov_b32_e32 v52, v2
	v_mov_b32_e32 v53, v20
	v_mov_b32_e32 v71, v61
	v_mov_b32_e32 v41, v27
	v_cvt_pk_f32_fp8_sdwa v[92:93], v24 src0_sel:WORD_1
	v_cvt_pk_f32_fp8_e32 v[94:95], v24
	v_pk_fma_f32 v[6:7], v[20:21], v[6:7], v[98:99] op_sel_hi:[0,1,1]
	v_pk_fma_f32 v[20:21], v[52:53], v[70:71], v[48:49]
	v_mov_b32_e32 v75, v26
	v_pk_fma_f32 v[26:27], v[18:19], v[40:41], v[50:51] op_sel:[1,0,0] op_sel_hi:[0,1,1]
	v_mov_b32_e32 v40, v3
	v_mov_b32_e32 v41, v18
	v_mov_b32_e32 v81, v57
	v_pk_mul_f32 v[76:77], v[2:3], v[76:77] op_sel:[1,0] op_sel_hi:[0,1]
	v_pk_fma_f32 v[6:7], v[18:19], v[64:65], v[6:7] op_sel_hi:[0,1,1]
	v_pk_fma_f32 v[44:45], v[18:19], v[74:75], v[44:45] op_sel:[1,0,0] op_sel_hi:[0,1,1]
	v_pk_fma_f32 v[18:19], v[40:41], v[80:81], v[20:21]
	v_mov_b32_e32 v89, v38
	v_mov_b32_e32 v76, v18
	v_mov_b32_e32 v91, v39
	v_pk_mul_f32 v[38:39], v[18:19], v[18:19]
	v_pk_add_f32 v[40:41], v[18:19], v[76:77]
	v_cvt_pk_f32_fp8_e32 v[58:59], v42
	v_cvt_pk_f32_fp8_sdwa v[42:43], v42 src0_sel:WORD_1
	v_pk_mul_f32 v[96:97], v[2:3], v[92:93] op_sel:[1,0] op_sel_hi:[0,1]
	v_pk_fma_f32 v[20:21], v[2:3], v[88:89], v[44:45] op_sel:[1,0,0] op_sel_hi:[0,1,1]
	v_mov_b32_e32 v39, v41
	v_mov_b32_e32 v57, v3
	v_mov_b32_e32 v44, v56
	v_mov_b32_e32 v45, v95
	v_pk_mul_f32 v[92:93], v[2:3], v[92:93]
	v_pk_fma_f32 v[26:27], v[2:3], v[90:91], v[26:27] op_sel:[1,0,0] op_sel_hi:[0,1,1]
	v_pk_fma_f32 v[38:39], v[56:57], v[44:45], v[38:39]
	v_mov_b32_e32 v44, v20
	v_mov_b32_e32 v45, v96
	v_add_f32_e32 v101, v0, v22
	v_mul_f32_e32 v0, v100, v100
	v_pk_add_f32 v[44:45], v[20:21], v[44:45]
	v_mov_b32_e32 v92, v26
	v_mul_f32_e32 v60, v101, v101
	v_pk_add_f32 v[48:49], v[26:27], v[92:93]
	v_pk_fma_f32 v[50:51], v[20:21], v[20:21], v[0:1]
	v_pk_mul_f32 v[52:53], v[44:45], v[44:45]
	v_pk_fma_f32 v[6:7], v[2:3], v[58:59], v[6:7] op_sel_hi:[0,1,1]
	v_pk_fma_f32 v[4:5], v[2:3], v[42:43], v[4:5] op_sel_hi:[0,1,1]
	v_mov_b32_e32 v51, v53
	v_pk_fma_f32 v[52:53], v[26:27], v[26:27], v[60:61]
	v_pk_mul_f32 v[54:55], v[48:49], v[48:49]
	v_pk_fma_f32 v[6:7], v[2:3], v[82:83], v[6:7] op_sel:[1,0,0]
	v_pk_fma_f32 v[4:5], v[2:3], v[84:85], v[4:5] op_sel:[1,0,0]
	v_mov_b32_e32 v53, v55
	v_pk_mul_f32 v[86:87], v[2:3], v[86:87] op_sel:[1,0] op_sel_hi:[0,1]
	v_pk_mul_f32 v[42:43], v[4:5], v[4:5]
	v_pk_add_f32 v[50:51], v[50:51], v[52:53]
	v_mov_b32_e32 v2, v6
	v_mov_b32_e32 v52, v6
	v_mov_b32_e32 v53, v94
	v_mul_f32_e32 v78, v7, v7
	v_mov_b32_e32 v54, v4
	v_mov_b32_e32 v55, v3
	v_mov_b32_e32 v58, v4
	v_mov_b32_e32 v59, v94
	v_pk_fma_f32 v[52:53], v[2:3], v[52:53], v[78:79]
	v_mov_b32_e32 v78, v43
	v_pk_fma_f32 v[42:43], v[54:55], v[58:59], v[78:79]
	v_pk_add_f32 v[54:55], v[52:53], v[42:43]
	v_pk_mul_f32 v[42:43], v[52:53], v[42:43]
	v_lshlrev_b32_e32 v0, 16, v1
	v_mov_b32_e32 v55, v43
	v_and_b32_e32 v1, 0xffff0000, v1
	v_mov_b32_e32 v42, v66
	v_mov_b32_e32 v43, v46
	v_pk_add_f32 v[0:1], v[42:43], v[0:1]
	v_mov_b32_e32 v46, v67
	v_pk_add_f32 v[0:1], v[0:1], v[46:47]
	v_mov_b32_e32 v42, v87
	v_mov_b32_e32 v43, v37
	v_pk_add_f32 v[0:1], v[0:1], v[42:43]
	v_mov_b32_e32 v87, v36
	v_pk_add_f32 v[36:37], v[0:1], v[86:87]
	v_mov_b32_e32 v27, v101
	v_pk_mul_f32 v[0:1], v[36:37], v[36:37]
	v_mov_b32_e32 v2, v37
	v_mov_b32_e32 v94, v37
	v_mov_b32_e32 v1, v41
	v_pk_fma_f32 v[0:1], v[2:3], v[94:95], v[0:1]
	v_lshl_add_u64 v[40:41], s[6:7], 0, v[8:9]
	v_pk_add_f32 v[2:3], v[38:39], v[0:1]
	v_pk_mul_f32 v[0:1], v[38:39], v[0:1]
	v_mov_b32_e32 v48, v45
	v_mov_b32_e32 v3, v1
	v_pk_add_f32 v[0:1], v[54:55], v[2:3]
	v_mov_b32_e32 v38, v53
	v_pk_add_f32 v[0:1], v[0:1], v[50:51]
	s_nop 0
	v_add_f32_e32 v0, v0, v1
	ds_bpermute_b32 v1, v28, v0
	s_waitcnt lgkmcnt(0)
	v_add_f32_e32 v0, v0, v1
	ds_bpermute_b32 v1, v29, v0
	s_waitcnt lgkmcnt(0)
	v_add_f32_e32 v0, v0, v1
	ds_bpermute_b32 v1, v30, v0
	s_waitcnt lgkmcnt(0)
	v_add_f32_e32 v0, v0, v1
	ds_bpermute_b32 v1, v31, v0
	s_waitcnt lgkmcnt(0)
	v_add_f32_e32 v0, v0, v1
	ds_bpermute_b32 v1, v32, v0
	s_waitcnt lgkmcnt(0)
	v_add_f32_e32 v0, v0, v1
	ds_bpermute_b32 v1, v33, v0
	s_waitcnt lgkmcnt(0)
	v_add_f32_e32 v0, v0, v1
	v_fmamk_f32 v0, v0, 0x3a800000, v34
	v_mul_f32_e32 v1, 0x4f800000, v0
	v_cmp_gt_f32_e32 vcc, s38, v0
	s_nop 1
	v_cndmask_b32_e32 v0, v0, v1, vcc
	v_sqrt_f32_e32 v1, v0
	s_nop 0
	v_add_u32_e32 v2, -1, v1
	v_fma_f32 v3, -v2, v1, v0
	v_cmp_ge_f32_e64 s[0:1], 0, v3
	v_add_u32_e32 v3, 1, v1
	s_nop 0
	v_cndmask_b32_e64 v2, v1, v2, s[0:1]
	v_fma_f32 v1, -v3, v1, v0
	v_cmp_lt_f32_e64 s[0:1], 0, v1
	s_nop 1
	v_cndmask_b32_e64 v1, v2, v3, s[0:1]
	v_mul_f32_e32 v2, 0x37800000, v1
	v_cndmask_b32_e32 v1, v1, v2, vcc
	v_cmp_class_f32_e32 vcc, v0, v35
	s_nop 1
	v_cndmask_b32_e32 v0, v1, v0, vcc
	v_div_scale_f32 v1, s[0:1], v0, v0, 1.0
	v_rcp_f32_e32 v2, v1
	s_nop 0
	v_fma_f32 v3, -v1, v2, 1.0
	v_fmac_f32_e32 v2, v3, v2
	v_div_scale_f32 v3, vcc, 1.0, v0, 1.0
	v_mul_f32_e32 v19, v3, v2
	v_fma_f32 v21, -v1, v19, v3
	v_fmac_f32_e32 v19, v21, v2
	v_fma_f32 v1, -v1, v19, v3
	v_div_fmas_f32 v1, v1, v2, v19
	v_div_fixup_f32 v42, v1, v0, 1.0
	v_pk_mul_f32 v[0:1], v[42:43], v[6:7] op_sel_hi:[0,1]
	v_pk_mul_f32 v[2:3], v[42:43], v[4:5] op_sel_hi:[0,1]
	s_waitcnt vmcnt(4)
	v_pk_mul_f32 v[2:3], v[202:203], v[2:3]
	v_pk_mul_f32 v[0:1], v[200:201], v[0:1]
	global_store_dwordx4 v[40:41], v[0:3], off nt
	v_mov_b32_e32 v19, v56
	v_pk_mul_f32 v[4:5], v[42:43], v[36:37] op_sel_hi:[0,1]
	v_pk_mul_f32 v[6:7], v[42:43], v[18:19] op_sel_hi:[0,1]
	v_mov_b32_e32 v21, v100
	v_pk_mul_f32 v[0:1], v[204:205], v[6:7]
	v_pk_mul_f32 v[2:3], v[206:207], v[4:5]
	global_store_dwordx4 v[40:41], v[0:3], off offset:1024 nt
	v_pk_mul_f32 v[4:5], v[42:43], v[26:27] op_sel_hi:[0,1]
	v_pk_mul_f32 v[6:7], v[42:43], v[20:21] op_sel_hi:[0,1]
	v_pk_mul_f32 v[0:1], v[208:209], v[6:7]
	v_pk_mul_f32 v[2:3], v[210:211], v[4:5]
	global_store_dwordx4 v[40:41], v[0:3], off offset:2048 nt
	v_pk_mul_f32 v[4:5], v[42:43], v[38:39] op_sel_hi:[0,1]
	v_pk_mul_f32 v[6:7], v[42:43], v[48:49] op_sel_hi:[0,1]
	v_pk_mul_f32 v[0:1], v[212:213], v[4:5]
	v_pk_mul_f32 v[2:3], v[214:215], v[6:7]
	global_store_dwordx4 v[40:41], v[0:3], off offset:3072 nt
	s_branch .LBB0_1396

	.amdhsa_kernel _Z6mk_fwd4Args
		.amdhsa_group_segment_fixed_size 0
		.amdhsa_private_segment_fixed_size 0
		.amdhsa_kernarg_size 440
		.amdhsa_user_sgpr_count 2
		.amdhsa_user_sgpr_dispatch_ptr 0
		.amdhsa_user_sgpr_queue_ptr 0
		.amdhsa_user_sgpr_kernarg_segment_ptr 1
		.amdhsa_user_sgpr_dispatch_id 0
		.amdhsa_user_sgpr_kernarg_preload_length 0
		.amdhsa_user_sgpr_kernarg_preload_offset 0
		.amdhsa_user_sgpr_private_segment_size 0
		.amdhsa_uses_dynamic_stack 0
		.amdhsa_enable_private_segment 0
		.amdhsa_system_sgpr_workgroup_id_x 1
		.amdhsa_system_sgpr_workgroup_id_y 0
		.amdhsa_system_sgpr_workgroup_id_z 0
		.amdhsa_system_sgpr_workgroup_info 0
		.amdhsa_system_vgpr_workitem_id 0
		.amdhsa_next_free_vgpr 256
		.amdhsa_next_free_sgpr 102
		.amdhsa_accum_offset 256
		.amdhsa_reserve_vcc 1
		.amdhsa_float_round_mode_32 0
		.amdhsa_float_round_mode_16_64 0
		.amdhsa_float_denorm_mode_32 3
		.amdhsa_float_denorm_mode_16_64 3
		.amdhsa_dx10_clamp 1
		.amdhsa_ieee_mode 1
		.amdhsa_fp16_overflow 0
		.amdhsa_tg_split 0
		.amdhsa_exception_fp_ieee_invalid_op 0
		.amdhsa_exception_fp_denorm_src 0
		.amdhsa_exception_fp_ieee_div_zero 0
		.amdhsa_exception_fp_ieee_overflow 0
		.amdhsa_exception_fp_ieee_underflow 0
		.amdhsa_exception_fp_ieee_inexact 0
		.amdhsa_exception_int_div_zero 0
	.end_amdhsa_kernel

.Lfunc_end0:
	.size	_Z6mk_fwd4Args, .Lfunc_end0-_Z6mk_fwd4Args
	.set _Z6mk_fwd4Args.num_vgpr, 256
	.set _Z6mk_fwd4Args.num_agpr, 0
	.set _Z6mk_fwd4Args.numbered_sgpr, 102
	.set _Z6mk_fwd4Args.num_named_barrier, 0
	.set _Z6mk_fwd4Args.private_seg_size, 0
	.set _Z6mk_fwd4Args.uses_vcc, 1
	.set _Z6mk_fwd4Args.uses_flat_scratch, 0
	.set _Z6mk_fwd4Args.has_dyn_sized_stack, 0
	.set _Z6mk_fwd4Args.has_recursion, 0
	.set _Z6mk_fwd4Args.has_indirect_call, 0

amdhsa.kernels:
  - .agpr_count:     0
    .args:
      - .offset:         0
        .size:           184
        .value_kind:     by_value
      - .offset:         184
        .size:           4
        .value_kind:     hidden_block_count_x
      - .offset:         188
        .size:           4
        .value_kind:     hidden_block_count_y
      - .offset:         192
        .size:           4
        .value_kind:     hidden_block_count_z
      - .offset:         196
        .size:           2
        .value_kind:     hidden_group_size_x
      - .offset:         198
        .size:           2
        .value_kind:     hidden_group_size_y
      - .offset:         200
        .size:           2
        .value_kind:     hidden_group_size_z
      - .offset:         202
        .size:           2
        .value_kind:     hidden_remainder_x
      - .offset:         204
        .size:           2
        .value_kind:     hidden_remainder_y
      - .offset:         206
        .size:           2
        .value_kind:     hidden_remainder_z
      - .offset:         224
        .size:           8
        .value_kind:     hidden_global_offset_x
      - .offset:         232
        .size:           8
        .value_kind:     hidden_global_offset_y
      - .offset:         240
        .size:           8
        .value_kind:     hidden_global_offset_z
      - .offset:         248
        .size:           2
        .value_kind:     hidden_grid_dims
      - .offset:         304
        .size:           4
        .value_kind:     hidden_dynamic_lds_size
    .group_segment_fixed_size: 0
    .kernarg_segment_align: 8
    .kernarg_segment_size: 440
    .language:       OpenCL C
    .language_version:
      - 2
      - 0
    .max_flat_workgroup_size: 512
    .name:           _Z6mk_fwd4Args
    .private_segment_fixed_size: 0
    .sgpr_count:     108
    .sgpr_spill_count: 105
    .symbol:         _Z6mk_fwd4Args.kd
    .uniform_work_group_size: 1
    .uses_dynamic_stack: false
    .vgpr_count:     256
    .vgpr_spill_count: 0
    .wavefront_size: 64
